# P9: nt policy on the once-read expert-output and residual row loads
# baseline (speedup 1.0000x reference)
; __device__ __forceinline__ float bf_lo(unsigned u) { return __uint_as_float(u << 16); }
; __device__ __forceinline__ float bf_hi(unsigned u) { return __uint_as_float(u & 0xffff0000u); }
; __device__ __forceinline__ void p9_final(Ctx& X) {
;     ...
;         const u32x2* hr = (const u32x2*)(XP_Hh(X) + (size_t)t * D) + lane;
;         f32x4 v[8];
; #pragma unroll
;         for (int j = 0; j < 8; ++j) { const u32x2 hv = hr[64 * j]; v[j] = (f32x4){bf_lo(hv.x), bf_hi(hv.x), bf_lo(hv.y), bf_hi(hv.y)}; }
; #pragma unroll
;         for (int k = 0; k < 4; ++k) { const int e = XP_TOPI(X)[t * 4 + k], r = XP_TOPR(X)[t * 4 + k]; const float wk = XP_TOPW(X)[t * 4 + k];
;             const unsigned* yr = (const unsigned*)(XP_YR(X) + ((size_t)tab[8 + e] * 256 + r) * D) + lane;
.LBB0_1128:
	s_ashr_i32 s7, s6, 31
	s_lshl_b64 s[20:21], s[6:7], 2
	s_add_u32 s22, s12, s20
	s_addc_u32 s23, s13, s21
	global_load_dwordx2 v[36:37], v[16:17], off nt
	global_load_dwordx2 v[40:41], v[16:17], off offset:512 nt
	global_load_dwordx2 v[42:43], v[16:17], off offset:1024 nt
	global_load_dwordx2 v[34:35], v[16:17], off offset:1536 nt
	global_load_dwordx2 v[30:31], v[16:17], off offset:2048 nt
	global_load_dwordx2 v[26:27], v[16:17], off offset:2560 nt
	global_load_dwordx2 v[22:23], v[16:17], off offset:3072 nt
	global_load_dwordx2 v[20:21], v[16:17], off offset:3584 nt
	global_load_dwordx4 v[56:59], v5, s[22:23]
	s_add_u32 s22, s14, s20
	s_addc_u32 s23, s15, s21
	s_add_u32 s20, s16, s20
	s_addc_u32 s21, s17, s21
	global_load_dword v64, v5, s[22:23]
	global_load_dword v28, v5, s[20:21]
	s_add_i32 s22, s6, 1
	s_ashr_i32 s23, s22, 31
	s_lshl_b64 s[20:21], s[22:23], 2
	s_add_u32 s22, s14, s20
	s_addc_u32 s23, s15, s21
	global_load_dwordx3 v[60:62], v5, s[22:23]
	s_add_u32 s20, s16, s20
	s_addc_u32 s21, s17, s21
	global_load_dword v4, v5, s[20:21]
	s_add_i32 s22, s6, 2
	s_ashr_i32 s23, s22, 31
	s_lshl_b64 s[20:21], s[22:23], 2
	s_add_u32 s20, s16, s20
	s_addc_u32 s21, s17, s21
	global_load_dwordx2 v[24:25], v5, s[20:21]
	s_add_i32 s2, s2, s4
	s_add_i32 s6, s6, s18
	v_lshl_add_u64 v[16:17], v[16:17], 0, s[8:9]
	s_cmpk_lt_i32 s2, 0x2000
	s_waitcnt vmcnt(0)
	v_lshlrev_b32_e32 v32, 16, v36
	v_and_b32_e32 v33, 0xffff0000, v36
	v_lshlrev_b32_e32 v36, 16, v37
	v_and_b32_e32 v37, 0xffff0000, v37
	v_lshlrev_b32_e32 v38, 16, v40
	v_and_b32_e32 v39, 0xffff0000, v40
	v_lshlrev_b32_e32 v40, 16, v41
	v_and_b32_e32 v41, 0xffff0000, v41
	v_lshlrev_b32_e32 v55, 2, v56
	v_lshlrev_b32_e32 v56, 2, v57
	v_lshlrev_b32_e32 v57, 2, v58
	v_lshlrev_b32_e32 v58, 2, v59
	v_add_u32_e32 v55, s3, v55
	v_add_u32_e32 v59, s3, v56
	v_add_u32_e32 v57, s3, v57
	v_add_u32_e32 v63, s3, v58
	ds_read_b32 v56, v55
	ds_read_b32 v58, v59
	ds_read_b32 v74, v57
	ds_read_b32 v76, v63
	v_ashrrev_i32_e32 v65, 31, v64
	s_waitcnt lgkmcnt(3)
	v_ashrrev_i32_e32 v57, 31, v56
	s_waitcnt lgkmcnt(2)
	v_ashrrev_i32_e32 v59, 31, v58
	s_waitcnt lgkmcnt(1)
	v_ashrrev_i32_e32 v75, 31, v74
	s_waitcnt lgkmcnt(0)
	v_ashrrev_i32_e32 v77, 31, v76
	v_lshlrev_b64 v[56:57], 19, v[56:57]
	v_lshlrev_b64 v[64:65], 11, v[64:65]
	v_ashrrev_i32_e32 v79, 31, v60
	v_mov_b32_e32 v78, v60
	v_lshlrev_b64 v[58:59], 19, v[58:59]
	v_ashrrev_i32_e32 v81, 31, v61
	v_mov_b32_e32 v80, v61
	v_lshlrev_b64 v[60:61], 19, v[74:75]
	v_ashrrev_i32_e32 v63, 31, v62
	v_lshlrev_b64 v[74:75], 19, v[76:77]
	v_lshl_add_u64 v[56:57], s[0:1], 0, v[56:57]
	v_lshlrev_b64 v[76:77], 11, v[78:79]
	v_lshl_add_u64 v[58:59], s[0:1], 0, v[58:59]
	v_lshlrev_b64 v[78:79], 11, v[80:81]
	v_lshl_add_u64 v[60:61], s[0:1], 0, v[60:61]
	v_lshlrev_b64 v[62:63], 11, v[62:63]
	v_lshl_add_u64 v[74:75], s[0:1], 0, v[74:75]
	v_lshl_add_u64 v[56:57], v[56:57], 0, v[64:65]
	v_lshl_add_u64 v[58:59], v[58:59], 0, v[76:77]
	v_lshl_add_u64 v[60:61], v[60:61], 0, v[78:79]
	v_lshl_add_u64 v[62:63], v[74:75], 0, v[62:63]
	v_readfirstlane_b32 s20, v56
	v_readfirstlane_b32 s21, v57
	v_readfirstlane_b32 s22, v58
	v_readfirstlane_b32 s23, v59
	v_readfirstlane_b32 s24, v60
	v_readfirstlane_b32 s25, v61
	v_readfirstlane_b32 s26, v62
	v_readfirstlane_b32 s27, v63
	global_load_dword v55, v53, s[20:21] nt
	global_load_dword v62, v53, s[20:21] offset:256 nt
	global_load_dword v74, v53, s[20:21] offset:512 nt
	global_load_dword v78, v53, s[20:21] offset:768 nt
	global_load_dword v82, v53, s[20:21] offset:1024 nt
	global_load_dword v86, v53, s[20:21] offset:1280 nt
	global_load_dword v90, v53, s[20:21] offset:1536 nt
	global_load_dword v94, v53, s[20:21] offset:1792 nt
	global_load_dword v98, v53, s[22:23] nt
	global_load_dword v102, v53, s[22:23] offset:256 nt
	global_load_dword v106, v53, s[22:23] offset:512 nt
	global_load_dword v110, v53, s[22:23] offset:768 nt
	global_load_dword v114, v53, s[22:23] offset:1024 nt
	global_load_dword v118, v53, s[22:23] offset:1280 nt
	global_load_dword v122, v53, s[22:23] offset:1536 nt
	global_load_dword v126, v53, s[22:23] offset:1792 nt
	global_load_dword v130, v53, s[24:25] nt
	global_load_dword v134, v53, s[24:25] offset:256 nt
	global_load_dword v138, v53, s[24:25] offset:512 nt
	global_load_dword v142, v53, s[24:25] offset:768 nt
	global_load_dword v146, v53, s[24:25] offset:1024 nt
	global_load_dword v150, v53, s[24:25] offset:1280 nt
	global_load_dword v154, v53, s[24:25] offset:1536 nt
	global_load_dword v158, v53, s[24:25] offset:1792 nt
	global_load_dword v162, v53, s[26:27] nt
	global_load_dword v166, v53, s[26:27] offset:256 nt
	global_load_dword v170, v53, s[26:27] offset:512 nt
	global_load_dword v174, v53, s[26:27] offset:768 nt
	global_load_dword v178, v53, s[26:27] offset:1024 nt
	global_load_dword v182, v53, s[26:27] offset:1280 nt
	global_load_dword v186, v53, s[26:27] offset:1536 nt
	global_load_dword v190, v53, s[26:27] offset:1792 nt
	v_lshlrev_b32_e32 v44, 16, v42
	v_and_b32_e32 v45, 0xffff0000, v42
	v_lshlrev_b32_e32 v42, 16, v43
	v_and_b32_e32 v43, 0xffff0000, v43
	v_lshlrev_b32_e32 v46, 16, v34
	v_and_b32_e32 v47, 0xffff0000, v34
	v_lshlrev_b32_e32 v34, 16, v35
	v_and_b32_e32 v35, 0xffff0000, v35
	v_lshlrev_b32_e32 v66, 16, v30
	v_and_b32_e32 v67, 0xffff0000, v30
	v_lshlrev_b32_e32 v30, 16, v31
	v_and_b32_e32 v31, 0xffff0000, v31
	v_lshlrev_b32_e32 v68, 16, v26
	v_and_b32_e32 v69, 0xffff0000, v26
	v_lshlrev_b32_e32 v26, 16, v27
	v_and_b32_e32 v27, 0xffff0000, v27
	v_lshlrev_b32_e32 v70, 16, v22
	v_and_b32_e32 v71, 0xffff0000, v22
	v_lshlrev_b32_e32 v22, 16, v23
	v_and_b32_e32 v23, 0xffff0000, v23
	v_lshlrev_b32_e32 v72, 16, v20
	v_and_b32_e32 v73, 0xffff0000, v20
	v_lshlrev_b32_e32 v20, 16, v21
	v_and_b32_e32 v21, 0xffff0000, v21
	s_waitcnt vmcnt(31)
; __device__ __forceinline__ void p9_final(Ctx& X) {
;     ...
;             for (int j = 0; j < 8; ++j) { const int y = (int)yr[64 * j]; const f32x2 lo = __builtin_amdgcn_cvt_pk_f32_fp8(y, false), hi = __builtin_amdgcn_cvt_pk_f32_fp8(y, true);
;                 v[j].x += wk * lo.x; v[j].y += wk * lo.y; v[j].z += wk * hi.x; v[j].w += wk * hi.y; } }
	v_cvt_pk_f32_fp8_e32 v[56:57], v55
	v_cvt_pk_f32_fp8_sdwa v[58:59], v55 src0_sel:WORD_1
	s_waitcnt vmcnt(30)
	v_cvt_pk_f32_fp8_e32 v[60:61], v62
	v_cvt_pk_f32_fp8_sdwa v[62:63], v62 src0_sel:WORD_1
	s_waitcnt vmcnt(29)
	v_cvt_pk_f32_fp8_e32 v[64:65], v74
	v_cvt_pk_f32_fp8_sdwa v[74:75], v74 src0_sel:WORD_1
	s_waitcnt vmcnt(28)
	v_cvt_pk_f32_fp8_e32 v[76:77], v78
	v_cvt_pk_f32_fp8_sdwa v[78:79], v78 src0_sel:WORD_1
	s_waitcnt vmcnt(23)
	v_cvt_pk_f32_fp8_e32 v[96:97], v98
	v_cvt_pk_f32_fp8_sdwa v[98:99], v98 src0_sel:WORD_1
	s_waitcnt vmcnt(22)
	v_cvt_pk_f32_fp8_e32 v[100:101], v102
	v_cvt_pk_f32_fp8_sdwa v[102:103], v102 src0_sel:WORD_1
	v_cvt_pk_f32_fp8_e32 v[80:81], v82
	v_cvt_pk_f32_fp8_sdwa v[82:83], v82 src0_sel:WORD_1
	v_cvt_pk_f32_fp8_e32 v[84:85], v86
	v_cvt_pk_f32_fp8_sdwa v[86:87], v86 src0_sel:WORD_1
	v_cvt_pk_f32_fp8_e32 v[88:89], v90
	v_cvt_pk_f32_fp8_sdwa v[90:91], v90 src0_sel:WORD_1
	v_cvt_pk_f32_fp8_e32 v[92:93], v94
	v_cvt_pk_f32_fp8_sdwa v[94:95], v94 src0_sel:WORD_1
	s_waitcnt vmcnt(21)
	v_cvt_pk_f32_fp8_e32 v[104:105], v106
	v_cvt_pk_f32_fp8_sdwa v[106:107], v106 src0_sel:WORD_1
	s_waitcnt vmcnt(15)
	v_cvt_pk_f32_fp8_e32 v[128:129], v130
	v_cvt_pk_f32_fp8_sdwa v[130:131], v130 src0_sel:WORD_1
	s_waitcnt vmcnt(14)
	v_cvt_pk_f32_fp8_e32 v[132:133], v134
	v_cvt_pk_f32_fp8_sdwa v[134:135], v134 src0_sel:WORD_1
	v_cvt_pk_f32_fp8_e32 v[108:109], v110
	v_cvt_pk_f32_fp8_sdwa v[110:111], v110 src0_sel:WORD_1
	v_cvt_pk_f32_fp8_e32 v[112:113], v114
	v_cvt_pk_f32_fp8_sdwa v[114:115], v114 src0_sel:WORD_1
	v_cvt_pk_f32_fp8_e32 v[116:117], v118
	v_cvt_pk_f32_fp8_sdwa v[118:119], v118 src0_sel:WORD_1
	v_cvt_pk_f32_fp8_e32 v[120:121], v122
	v_cvt_pk_f32_fp8_sdwa v[122:123], v122 src0_sel:WORD_1
	v_cvt_pk_f32_fp8_e32 v[124:125], v126
	v_cvt_pk_f32_fp8_sdwa v[126:127], v126 src0_sel:WORD_1
	s_waitcnt vmcnt(13)
	v_cvt_pk_f32_fp8_e32 v[136:137], v138
	v_cvt_pk_f32_fp8_sdwa v[138:139], v138 src0_sel:WORD_1
	s_waitcnt vmcnt(7)
	v_cvt_pk_f32_fp8_e32 v[160:161], v162
	v_cvt_pk_f32_fp8_sdwa v[162:163], v162 src0_sel:WORD_1
	s_waitcnt vmcnt(6)
	v_cvt_pk_f32_fp8_e32 v[164:165], v166
	v_cvt_pk_f32_fp8_sdwa v[166:167], v166 src0_sel:WORD_1
	v_cvt_pk_f32_fp8_e32 v[140:141], v142
	v_cvt_pk_f32_fp8_sdwa v[142:143], v142 src0_sel:WORD_1
	v_cvt_pk_f32_fp8_e32 v[144:145], v146
	v_cvt_pk_f32_fp8_sdwa v[146:147], v146 src0_sel:WORD_1
	v_cvt_pk_f32_fp8_e32 v[148:149], v150
	v_cvt_pk_f32_fp8_sdwa v[150:151], v150 src0_sel:WORD_1
	v_cvt_pk_f32_fp8_e32 v[152:153], v154
	v_cvt_pk_f32_fp8_sdwa v[154:155], v154 src0_sel:WORD_1
	v_cvt_pk_f32_fp8_e32 v[156:157], v158
	v_cvt_pk_f32_fp8_sdwa v[158:159], v158 src0_sel:WORD_1
	s_waitcnt vmcnt(5)
	v_cvt_pk_f32_fp8_e32 v[168:169], v170
	v_cvt_pk_f32_fp8_sdwa v[170:171], v170 src0_sel:WORD_1
	v_pk_fma_f32 v[32:33], v[28:29], v[56:57], v[32:33] op_sel_hi:[0,1,1]
	v_pk_fma_f32 v[36:37], v[28:29], v[58:59], v[36:37] op_sel_hi:[0,1,1]
	v_pk_fma_f32 v[38:39], v[28:29], v[60:61], v[38:39] op_sel_hi:[0,1,1]
	v_pk_fma_f32 v[40:41], v[28:29], v[62:63], v[40:41] op_sel_hi:[0,1,1]
	s_waitcnt vmcnt(4)
	v_cvt_pk_f32_fp8_e32 v[172:173], v174
	v_cvt_pk_f32_fp8_sdwa v[174:175], v174 src0_sel:WORD_1
	s_waitcnt vmcnt(3)
	v_cvt_pk_f32_fp8_e32 v[176:177], v178
	v_cvt_pk_f32_fp8_sdwa v[178:179], v178 src0_sel:WORD_1
	s_waitcnt vmcnt(2)
	v_cvt_pk_f32_fp8_e32 v[180:181], v182
	v_cvt_pk_f32_fp8_sdwa v[182:183], v182 src0_sel:WORD_1
	s_waitcnt vmcnt(1)
	v_cvt_pk_f32_fp8_e32 v[184:185], v186
	v_cvt_pk_f32_fp8_sdwa v[186:187], v186 src0_sel:WORD_1
	s_waitcnt vmcnt(0)
	v_cvt_pk_f32_fp8_e32 v[188:189], v190
	v_cvt_pk_f32_fp8_sdwa v[190:191], v190 src0_sel:WORD_1
	v_pk_fma_f32 v[44:45], v[28:29], v[64:65], v[44:45] op_sel_hi:[0,1,1]
	v_pk_fma_f32 v[42:43], v[28:29], v[74:75], v[42:43] op_sel_hi:[0,1,1]
	v_pk_fma_f32 v[32:33], v[4:5], v[96:97], v[32:33] op_sel_hi:[0,1,1]
	v_pk_fma_f32 v[36:37], v[4:5], v[98:99], v[36:37] op_sel_hi:[0,1,1]
	v_pk_fma_f32 v[38:39], v[4:5], v[100:101], v[38:39] op_sel_hi:[0,1,1]
	v_pk_fma_f32 v[40:41], v[4:5], v[102:103], v[40:41] op_sel_hi:[0,1,1]
	v_pk_fma_f32 v[46:47], v[28:29], v[76:77], v[46:47] op_sel_hi:[0,1,1]
	v_pk_fma_f32 v[34:35], v[28:29], v[78:79], v[34:35] op_sel_hi:[0,1,1]
	v_pk_fma_f32 v[56:57], v[28:29], v[80:81], v[66:67] op_sel_hi:[0,1,1]
	v_pk_fma_f32 v[30:31], v[28:29], v[82:83], v[30:31] op_sel_hi:[0,1,1]
	v_pk_fma_f32 v[58:59], v[28:29], v[84:85], v[68:69] op_sel_hi:[0,1,1]
	v_pk_fma_f32 v[26:27], v[28:29], v[86:87], v[26:27] op_sel_hi:[0,1,1]
	v_pk_fma_f32 v[60:61], v[28:29], v[88:89], v[70:71] op_sel_hi:[0,1,1]
	v_pk_fma_f32 v[22:23], v[28:29], v[90:91], v[22:23] op_sel_hi:[0,1,1]
	v_pk_fma_f32 v[62:63], v[28:29], v[92:93], v[72:73] op_sel_hi:[0,1,1]
	v_pk_fma_f32 v[20:21], v[28:29], v[94:95], v[20:21] op_sel_hi:[0,1,1]
	v_pk_fma_f32 v[44:45], v[4:5], v[104:105], v[44:45] op_sel_hi:[0,1,1]
	v_pk_fma_f32 v[42:43], v[4:5], v[106:107], v[42:43] op_sel_hi:[0,1,1]
	v_pk_fma_f32 v[32:33], v[24:25], v[128:129], v[32:33] op_sel_hi:[0,1,1]
	v_pk_fma_f32 v[36:37], v[24:25], v[130:131], v[36:37] op_sel_hi:[0,1,1]
	v_pk_fma_f32 v[38:39], v[24:25], v[132:133], v[38:39] op_sel_hi:[0,1,1]
	v_pk_fma_f32 v[40:41], v[24:25], v[134:135], v[40:41] op_sel_hi:[0,1,1]
	v_pk_fma_f32 v[46:47], v[4:5], v[108:109], v[46:47] op_sel_hi:[0,1,1]
	v_pk_fma_f32 v[34:35], v[4:5], v[110:111], v[34:35] op_sel_hi:[0,1,1]
	v_pk_fma_f32 v[56:57], v[4:5], v[112:113], v[56:57] op_sel_hi:[0,1,1]
	v_pk_fma_f32 v[30:31], v[4:5], v[114:115], v[30:31] op_sel_hi:[0,1,1]
	v_pk_fma_f32 v[58:59], v[4:5], v[116:117], v[58:59] op_sel_hi:[0,1,1]
	v_pk_fma_f32 v[26:27], v[4:5], v[118:119], v[26:27] op_sel_hi:[0,1,1]
; __device__ __forceinline__ float wave_sum(float v) {
;     ...
;     for (int o = 1; o < 64; o <<= 1) v += __shfl_xor(v, o);
; __device__ __forceinline__ void p9_final(Ctx& X) {
;     ...
;                 v[j].x += wk * lo.x; v[j].y += wk * lo.y; v[j].z += wk * hi.x; v[j].w += wk * hi.y; } }
;         float s = 0.f;
; #pragma unroll
;         for (int j = 0; j < 8; ++j) s += (v[j].x * v[j].x + v[j].y * v[j].y) + (v[j].z * v[j].z + v[j].w * v[j].w);
;         const float rstd = rsqrtf(wave_sum(s) * (1.f / D) + EPS);
	v_pk_fma_f32 v[60:61], v[4:5], v[120:121], v[60:61] op_sel_hi:[0,1,1]
	v_pk_fma_f32 v[22:23], v[4:5], v[122:123], v[22:23] op_sel_hi:[0,1,1]
	v_pk_fma_f32 v[62:63], v[4:5], v[124:125], v[62:63] op_sel_hi:[0,1,1]
	v_pk_fma_f32 v[20:21], v[4:5], v[126:127], v[20:21] op_sel_hi:[0,1,1]
	v_pk_fma_f32 v[44:45], v[24:25], v[136:137], v[44:45] op_sel_hi:[0,1,1]
	v_pk_fma_f32 v[42:43], v[24:25], v[138:139], v[42:43] op_sel_hi:[0,1,1]
	v_pk_fma_f32 v[32:33], v[24:25], v[160:161], v[32:33] op_sel:[1,0,0]
	v_pk_fma_f32 v[36:37], v[24:25], v[162:163], v[36:37] op_sel:[1,0,0]
	v_pk_fma_f32 v[38:39], v[24:25], v[164:165], v[38:39] op_sel:[1,0,0]
	v_pk_fma_f32 v[40:41], v[24:25], v[166:167], v[40:41] op_sel:[1,0,0]
	v_pk_fma_f32 v[46:47], v[24:25], v[140:141], v[46:47] op_sel_hi:[0,1,1]
	v_pk_fma_f32 v[34:35], v[24:25], v[142:143], v[34:35] op_sel_hi:[0,1,1]
	v_pk_fma_f32 v[56:57], v[24:25], v[144:145], v[56:57] op_sel_hi:[0,1,1]
	v_pk_fma_f32 v[30:31], v[24:25], v[146:147], v[30:31] op_sel_hi:[0,1,1]
	v_pk_fma_f32 v[58:59], v[24:25], v[148:149], v[58:59] op_sel_hi:[0,1,1]
	v_pk_fma_f32 v[26:27], v[24:25], v[150:151], v[26:27] op_sel_hi:[0,1,1]
	v_pk_fma_f32 v[60:61], v[24:25], v[152:153], v[60:61] op_sel_hi:[0,1,1]
	v_pk_fma_f32 v[22:23], v[24:25], v[154:155], v[22:23] op_sel_hi:[0,1,1]
	v_pk_fma_f32 v[62:63], v[24:25], v[156:157], v[62:63] op_sel_hi:[0,1,1]
	v_pk_fma_f32 v[20:21], v[24:25], v[158:159], v[20:21] op_sel_hi:[0,1,1]
	v_pk_fma_f32 v[44:45], v[24:25], v[168:169], v[44:45] op_sel:[1,0,0]
	v_pk_fma_f32 v[42:43], v[24:25], v[170:171], v[42:43] op_sel:[1,0,0]
	v_mov_b32_e32 v64, v33
	v_mov_b32_e32 v65, v39
	v_mov_b32_e32 v68, v37
	v_mov_b32_e32 v69, v41
	v_pk_fma_f32 v[46:47], v[24:25], v[172:173], v[46:47] op_sel:[1,0,0]
	v_pk_fma_f32 v[34:35], v[24:25], v[174:175], v[34:35] op_sel:[1,0,0]
	v_pk_fma_f32 v[56:57], v[24:25], v[176:177], v[56:57] op_sel:[1,0,0]
	v_pk_fma_f32 v[30:31], v[24:25], v[178:179], v[30:31] op_sel:[1,0,0]
	v_pk_fma_f32 v[58:59], v[24:25], v[180:181], v[58:59] op_sel:[1,0,0]
	v_pk_fma_f32 v[26:27], v[24:25], v[182:183], v[26:27] op_sel:[1,0,0]
	v_pk_fma_f32 v[60:61], v[24:25], v[184:185], v[60:61] op_sel:[1,0,0]
	v_pk_fma_f32 v[22:23], v[24:25], v[186:187], v[22:23] op_sel:[1,0,0]
	v_pk_fma_f32 v[62:63], v[24:25], v[188:189], v[62:63] op_sel:[1,0,0]
	v_pk_fma_f32 v[20:21], v[24:25], v[190:191], v[20:21] op_sel:[1,0,0]
	v_mov_b32_e32 v24, v32
	v_mov_b32_e32 v25, v38
	v_mov_b32_e32 v66, v36
	v_mov_b32_e32 v67, v40
	v_mov_b32_e32 v72, v45
	v_mov_b32_e32 v73, v43
	v_pk_mul_f32 v[64:65], v[64:65], v[64:65]
	v_pk_mul_f32 v[68:69], v[68:69], v[68:69]
	v_mov_b32_e32 v70, v44
	v_mov_b32_e32 v71, v42
	v_pk_mul_f32 v[72:73], v[72:73], v[72:73]
	v_pk_fma_f32 v[24:25], v[24:25], v[24:25], v[64:65]
	v_pk_fma_f32 v[64:65], v[66:67], v[66:67], v[68:69]
	v_mul_f32_e32 v4, v47, v47
	v_mul_f32_e32 v28, v35, v35
	v_pk_fma_f32 v[66:67], v[70:71], v[70:71], v[72:73]
	v_pk_add_f32 v[24:25], v[24:25], v[64:65]
	v_pk_mul_f32 v[74:75], v[56:57], v[56:57]
	v_pk_mul_f32 v[76:77], v[30:31], v[30:31]
	v_pk_fma_f32 v[90:91], v[46:47], v[46:47], v[4:5] op_sel_hi:[1,1,0]
	v_pk_fma_f32 v[92:93], v[34:35], v[34:35], v[28:29] op_sel_hi:[1,1,0]
	v_pk_add_f32 v[64:65], v[66:67], v[66:67] op_sel:[0,1] op_sel_hi:[1,0]
	v_pk_add_f32 v[24:25], v[24:25], v[24:25] op_sel:[0,1] op_sel_hi:[1,0]
	v_mov_b32_e32 v80, v59
	v_mov_b32_e32 v81, v27
	v_mov_b32_e32 v91, v76
	v_mov_b32_e32 v93, v77
	v_mov_b32_e32 v65, v75
	v_mov_b32_e32 v25, v74
	v_mov_b32_e32 v78, v58
	v_mov_b32_e32 v79, v26
	v_pk_mul_f32 v[80:81], v[80:81], v[80:81]
	v_pk_add_f32 v[66:67], v[90:91], v[92:93]
	v_pk_add_f32 v[24:25], v[24:25], v[64:65]
	v_mul_f32_e32 v82, v61, v61
	v_mul_f32_e32 v84, v23, v23
	v_pk_fma_f32 v[68:69], v[78:79], v[78:79], v[80:81]
	v_pk_add_f32 v[24:25], v[24:25], v[66:67]
	v_pk_mul_f32 v[86:87], v[62:63], v[62:63]
	v_pk_mul_f32 v[88:89], v[20:21], v[20:21]
	v_pk_fma_f32 v[82:83], v[60:61], v[60:61], v[82:83] op_sel_hi:[1,1,0]
	v_pk_fma_f32 v[84:85], v[22:23], v[22:23], v[84:85] op_sel_hi:[1,1,0]
	v_pk_add_f32 v[68:69], v[68:69], v[68:69] op_sel:[0,1] op_sel_hi:[1,0]
	v_pk_add_f32 v[24:25], v[24:25], v[24:25] op_sel:[0,1] op_sel_hi:[1,0]
	v_mov_b32_e32 v83, v88
	v_mov_b32_e32 v85, v89
	v_mov_b32_e32 v69, v87
	v_mov_b32_e32 v25, v86
	v_pk_add_f32 v[70:71], v[82:83], v[84:85]
	v_pk_add_f32 v[24:25], v[24:25], v[68:69]
	s_nop 0
	v_pk_add_f32 v[24:25], v[24:25], v[70:71]
	s_nop 0
	v_add_f32_e32 v4, v24, v25
	ds_bpermute_b32 v24, v29, v4
	s_waitcnt lgkmcnt(0)
; __device__ __forceinline__ float wave_sum(float v) {
;     ...
;     for (int o = 1; o < 64; o <<= 1) v += __shfl_xor(v, o);
; __device__ __forceinline__ void p9_final(Ctx& X) {
;     ...
;         const float rstd = rsqrtf(wave_sum(s) * (1.f / D) + EPS);
;         f32x4* o = (f32x4*)(X.out + (size_t)t * D) + lane; const f32x4* wr_ = (const f32x4*)XP_ln_final_w(X) + lane;
; #pragma unroll
;         for (int j = 0; j < 8; ++j) { const f32x4 wv = wr_[64 * j]; f32x4 r; r.x = v[j].x * rstd * wv.x; r.y = v[j].y * rstd * wv.y; r.z = v[j].z * rstd * wv.z; r.w = v[j].w * rstd * wv.w; __builtin_nontemporal_store(r, &o[64 * j]); }
	v_add_f32_e32 v4, v4, v24
	ds_bpermute_b32 v24, v48, v4
	s_waitcnt lgkmcnt(0)
	v_add_f32_e32 v4, v4, v24
	ds_bpermute_b32 v24, v49, v4
	s_waitcnt lgkmcnt(0)
	v_add_f32_e32 v4, v4, v24
	ds_bpermute_b32 v24, v50, v4
	s_waitcnt lgkmcnt(0)
	v_add_f32_e32 v4, v4, v24
	ds_bpermute_b32 v24, v51, v4
	s_waitcnt lgkmcnt(0)
	v_add_f32_e32 v4, v4, v24
	ds_bpermute_b32 v24, v52, v4
	s_waitcnt lgkmcnt(0)
	v_add_f32_e32 v4, v4, v24
	v_fmamk_f32 v4, v4, 0x3a000000, v54
	v_mul_f32_e32 v24, 0x4b800000, v4
	v_cmp_gt_f32_e32 vcc, s5, v4
	s_nop 1
	v_cndmask_b32_e32 v4, v4, v24, vcc
	v_rsq_f32_e32 v4, v4
	s_nop 0
	v_mul_f32_e32 v24, 0x45800000, v4
	v_cndmask_b32_e32 v4, v4, v24, vcc
	v_pk_mul_f32 v[24:25], v[32:33], v[4:5] op_sel_hi:[1,0]
	v_pk_mul_f32 v[32:33], v[36:37], v[4:5] op_sel_hi:[1,0]
	v_pk_mul_f32 v[228:229], v[196:197], v[24:25]
	v_pk_mul_f32 v[230:231], v[198:199], v[32:33]
	global_store_dwordx4 v[18:19], v[228:231], off offset:-4096 nt
	v_pk_mul_f32 v[24:25], v[40:41], v[4:5] op_sel_hi:[1,0]
	v_pk_mul_f32 v[32:33], v[38:39], v[4:5] op_sel_hi:[1,0]
	v_pk_mul_f32 v[22:23], v[22:23], v[4:5] op_sel_hi:[1,0]
	v_pk_mul_f32 v[20:21], v[20:21], v[4:5] op_sel_hi:[1,0]
	v_pk_mul_f32 v[232:233], v[200:201], v[32:33]
	v_pk_mul_f32 v[234:235], v[202:203], v[24:25]
	global_store_dwordx4 v[18:19], v[232:235], off offset:-3072 nt
	v_pk_mul_f32 v[24:25], v[42:43], v[4:5] op_sel_hi:[1,0]
	v_pk_mul_f32 v[32:33], v[44:45], v[4:5] op_sel_hi:[1,0]
	v_pk_mul_f32 v[230:231], v[206:207], v[24:25]
	v_pk_mul_f32 v[228:229], v[204:205], v[32:33]
	global_store_dwordx4 v[18:19], v[228:231], off offset:-2048 nt
	v_pk_mul_f32 v[24:25], v[34:35], v[4:5] op_sel_hi:[1,0]
	v_pk_mul_f32 v[32:33], v[46:47], v[4:5] op_sel_hi:[1,0]
	v_pk_mul_f32 v[234:235], v[210:211], v[24:25]
	v_pk_mul_f32 v[232:233], v[208:209], v[32:33]
	global_store_dwordx4 v[18:19], v[232:235], off offset:-1024 nt
	v_pk_mul_f32 v[24:25], v[30:31], v[4:5] op_sel_hi:[1,0]
	v_pk_mul_f32 v[30:31], v[56:57], v[4:5] op_sel_hi:[1,0]
	v_pk_mul_f32 v[230:231], v[214:215], v[24:25]
	v_pk_mul_f32 v[228:229], v[212:213], v[30:31]
	global_store_dwordx4 v[18:19], v[228:231], off nt
	v_pk_mul_f32 v[24:25], v[26:27], v[4:5] op_sel_hi:[1,0]
	v_pk_mul_f32 v[26:27], v[58:59], v[4:5] op_sel_hi:[1,0]
	v_pk_mul_f32 v[234:235], v[218:219], v[24:25]
	v_pk_mul_f32 v[232:233], v[216:217], v[26:27]
	global_store_dwordx4 v[18:19], v[232:235], off offset:1024 nt
	v_pk_mul_f32 v[24:25], v[60:61], v[4:5] op_sel_hi:[1,0]
	v_pk_mul_f32 v[230:231], v[22:23], v[222:223]
	v_pk_mul_f32 v[228:229], v[24:25], v[220:221]
	global_store_dwordx4 v[18:19], v[228:231], off offset:2048 nt
	v_pk_mul_f32 v[22:23], v[62:63], v[4:5] op_sel_hi:[1,0]
	v_pk_mul_f32 v[234:235], v[20:21], v[226:227]
	v_pk_mul_f32 v[232:233], v[22:23], v[224:225]
	global_store_dwordx4 v[18:19], v[232:235], off offset:3072 nt
	v_lshl_add_u64 v[18:19], v[18:19], 0, s[10:11]
	s_cbranch_scc1 .LBB0_1128
